# the four MoE expert-weight conversion loops: per-row int8 scale loads issued in front of the item's weight-load wait, per-row vmcnt(0) drains removed
# baseline (speedup 1.0000x reference)
.LBB0_978:
	s_or_b64 exec, exec, s[4:5]
	s_mul_i32 s5, s8, 0x1600000
	s_mul_hi_i32 s4, s8, 0x1600000
	s_add_u32 s28, s12, s5
	s_addc_u32 s29, s14, s4
	s_mul_i32 s4, s8, 0x2c00
	s_ashr_i32 s5, s4, 31
	s_lshl_b64 s[4:5], s[4:5], 2
	s_add_u32 s4, s15, s4
	s_addc_u32 s5, s16, s5
	v_mov_b32_e32 v181, s26
	v_lshlrev_b32_e32 v181, 6, v181
	v_and_b32_e32 v181, 0xffffff00, v181
	v_or_b32_e32 v180, s27, v73
	v_and_b32_e32 v180, 0x67, v180
	v_or_b32_e32 v180, v181, v180
	v_or_b32_e32 v182, 0x80, v180
	v_cndmask_b32_e64 v182, v180, v182, s[6:7]
	v_ashrrev_i32_e32 v183, 31, v182
	v_lshl_add_u64 v[184:185], v[182:183], 2, s[4:5]
	global_load_dword v176, v[184:185], off
	v_or_b32_e32 v180, s27, v74
	v_and_b32_e32 v180, 0x6f, v180
	v_or_b32_e32 v180, v181, v180
	v_or_b32_e32 v182, 0x80, v180
	v_cndmask_b32_e64 v182, v180, v182, s[6:7]
	v_ashrrev_i32_e32 v183, 31, v182
	v_lshl_add_u64 v[184:185], v[182:183], 2, s[4:5]
	global_load_dword v177, v[184:185], off
	v_or_b32_e32 v180, s27, v75
	v_and_b32_e32 v180, 0x77, v180
	v_or_b32_e32 v180, v181, v180
	v_or_b32_e32 v182, 0x80, v180
	v_cndmask_b32_e64 v182, v180, v182, s[6:7]
	v_ashrrev_i32_e32 v183, 31, v182
	v_lshl_add_u64 v[184:185], v[182:183], 2, s[4:5]
	global_load_dword v178, v[184:185], off
	v_or_b32_e32 v180, s27, v76
	v_and_b32_e32 v180, 0x7f, v180
	v_or_b32_e32 v180, v181, v180
	v_or_b32_e32 v182, 0x80, v180
	v_cndmask_b32_e64 v182, v180, v182, s[6:7]
	v_ashrrev_i32_e32 v183, 31, v182
	v_lshl_add_u64 v[184:185], v[182:183], 2, s[4:5]
	global_load_dword v179, v[184:185], off
	s_waitcnt vmcnt(0)
	ds_write2_b32 v78, v6, v7 offset1:1
	ds_write2_b32 v78, v8, v9 offset0:2 offset1:3
	ds_write2_b32 v79, v2, v3 offset1:1
	ds_write2_b32 v80, v4, v5 offset1:1
	ds_write2_b32 v81, v14, v15 offset1:1
	ds_write2_b32 v82, v16, v17 offset1:1
	ds_write2_b32 v83, v10, v11 offset1:1
	ds_write2_b32 v84, v12, v13 offset1:1
	ds_write2_b32 v85, v22, v23 offset1:1
	ds_write2_b32 v86, v24, v25 offset1:1
	ds_write2_b32 v87, v18, v19 offset1:1
	ds_write2_b32 v88, v20, v21 offset1:1
	ds_write2_b32 v89, v30, v31 offset1:1
	ds_write2_b32 v90, v32, v33 offset1:1
	ds_write2_b32 v91, v26, v27 offset1:1
	ds_write2_b32 v92, v28, v29 offset1:1
	ds_write2_b32 v93, v38, v39 offset1:1
	ds_write2_b32 v94, v40, v41 offset1:1
	ds_write2_b32 v95, v34, v35 offset1:1
	ds_write2_b32 v96, v36, v37 offset1:1
	ds_write2_b32 v97, v46, v47 offset1:1
	ds_write2_b32 v98, v48, v49 offset1:1
	ds_write2_b32 v99, v42, v43 offset1:1
	ds_write2_b32 v100, v44, v45 offset1:1
	ds_write2_b32 v101, v54, v55 offset1:1
	ds_write2_b32 v102, v56, v57 offset1:1
	ds_write2_b32 v103, v50, v51 offset1:1
	ds_write2_b32 v104, v52, v53 offset1:1
	ds_write2_b32 v105, v62, v63 offset1:1
	ds_write2_b32 v106, v64, v65 offset1:1
	ds_write2_b32 v107, v58, v59 offset1:1
	ds_write2_b32 v108, v60, v61 offset1:1
	s_nop 0
	s_waitcnt lgkmcnt(0)
	s_ashr_i32 s30, s9, 31
	s_add_u32 s8, s28, s9
	s_addc_u32 s9, s29, s30
	v_or_b32_e32 v4, s27, v73
	v_lshl_add_u64 v[2:3], s[8:9], 0, v[66:67]
	v_cmp_gt_i32_e32 vcc, s23, v4
	s_and_saveexec_b64 s[8:9], vcc
	s_cbranch_execz .LBB0_980
	s_lshl_b32 s28, s26, 6
	s_and_b32 s28, s28, 0xffffff00
	v_and_b32_e32 v4, 0x67, v4
	v_or_b32_e32 v4, s28, v4
	v_or_b32_e32 v5, 0x80, v4
	v_cndmask_b32_e64 v4, v4, v5, s[6:7]
	v_ashrrev_i32_e32 v5, 31, v4
	v_lshl_add_u64 v[6:7], v[4:5], 2, s[4:5]
	v_mov_b32_e32 v24, v176
	v_lshlrev_b64 v[22:23], 11, v[4:5]
	ds_read2_b32 v[6:7], v77 offset1:33
	ds_read2_b32 v[8:9], v77 offset0:66 offset1:99
	ds_read2_b32 v[10:11], v77 offset0:132 offset1:165
	ds_read2_b32 v[12:13], v77 offset0:198 offset1:231
	ds_read2_b32 v[14:15], v109 offset0:8 offset1:41
	ds_read2_b32 v[16:17], v109 offset0:74 offset1:107
	ds_read2_b32 v[18:19], v109 offset0:140 offset1:173
	ds_read2_b32 v[20:21], v109 offset0:206 offset1:239
	s_nop 0
	v_div_scale_f32 v25, s[28:29], v24, v24, 1.0
	v_rcp_f32_e32 v26, v25
	v_div_scale_f32 v4, vcc, 1.0, v24, 1.0
	v_fma_f32 v5, -v25, v26, 1.0
	v_fmac_f32_e32 v26, v5, v26
	v_mul_f32_e32 v5, v4, v26
	v_fma_f32 v27, -v25, v5, v4
	v_fmac_f32_e32 v5, v27, v26
	v_fma_f32 v4, -v25, v5, v4
	v_div_fmas_f32 v4, v4, v26, v5
	v_div_fixup_f32 v4, v4, v24, 1.0
	s_waitcnt lgkmcnt(7)
	v_fmaak_f32 v5, v6, v4, 0x43000000
	v_fmaak_f32 v6, v4, v7, 0x43000000
	s_waitcnt lgkmcnt(6)
	v_fmaak_f32 v7, v4, v8, 0x43000000
	v_fmaak_f32 v8, v4, v9, 0x43000000
	s_waitcnt lgkmcnt(5)
	v_fmaak_f32 v9, v4, v10, 0x43000000
	v_fmaak_f32 v10, v4, v11, 0x43000000
	s_waitcnt lgkmcnt(4)
	v_fmaak_f32 v11, v4, v12, 0x43000000
	v_fmaak_f32 v12, v4, v13, 0x43000000
	s_waitcnt lgkmcnt(3)
	v_fmaak_f32 v13, v4, v14, 0x43000000
	v_fmaak_f32 v14, v4, v15, 0x43000000
	s_waitcnt lgkmcnt(2)
	v_fmaak_f32 v15, v4, v16, 0x43000000
	v_fmaak_f32 v16, v4, v17, 0x43000000
	s_waitcnt lgkmcnt(1)
	v_fmaak_f32 v17, v4, v18, 0x43000000
	v_fmaak_f32 v18, v4, v19, 0x43000000
	v_rndne_f32_e32 v5, v5
	v_rndne_f32_e32 v9, v9
	v_rndne_f32_e32 v13, v13
	v_rndne_f32_e32 v17, v17
	s_waitcnt lgkmcnt(0)
	v_fmaak_f32 v19, v4, v20, 0x43000000
	v_rndne_f32_e32 v6, v6
	v_rndne_f32_e32 v10, v10
	v_rndne_f32_e32 v14, v14
	v_rndne_f32_e32 v18, v18
	v_cvt_pk_u8_f32 v5, v5, 0, 0
	v_cvt_pk_u8_f32 v9, v9, 0, 0
	v_cvt_pk_u8_f32 v13, v13, 0, 0
	v_cvt_pk_u8_f32 v17, v17, 0, 0
	v_fmaak_f32 v4, v4, v21, 0x43000000
	v_rndne_f32_e32 v7, v7
	v_rndne_f32_e32 v11, v11
	v_rndne_f32_e32 v15, v15
	v_rndne_f32_e32 v19, v19
	v_cvt_pk_u8_f32 v5, v6, 1, v5
	v_cvt_pk_u8_f32 v6, v10, 1, v9
	v_cvt_pk_u8_f32 v9, v14, 1, v13
	v_cvt_pk_u8_f32 v10, v18, 1, v17
	v_rndne_f32_e32 v8, v8
	v_rndne_f32_e32 v12, v12
	v_rndne_f32_e32 v16, v16
	v_rndne_f32_e32 v4, v4
	v_cvt_pk_u8_f32 v5, v7, 2, v5
	v_cvt_pk_u8_f32 v6, v11, 2, v6
	v_cvt_pk_u8_f32 v7, v15, 2, v9
	v_cvt_pk_u8_f32 v9, v19, 2, v10
	v_cvt_pk_u8_f32 v5, v8, 3, v5
	v_cvt_pk_u8_f32 v6, v12, 3, v6
	v_cvt_pk_u8_f32 v7, v16, 3, v7
	v_cvt_pk_u8_f32 v8, v4, 3, v9
	v_xor_b32_e32 v4, 0x80808080, v5
	v_xor_b32_e32 v5, 0x80808080, v6
	v_xor_b32_e32 v6, 0x80808080, v7
	v_xor_b32_e32 v7, 0x80808080, v8
	v_lshl_add_u64 v[8:9], v[2:3], 0, v[22:23]
	global_store_dwordx4 v[8:9], v[4:7], off nt
.LBB0_980:
	s_or_b64 exec, exec, s[8:9]
	s_nop 0
	v_or_b32_e32 v4, s27, v74
	v_cmp_gt_i32_e32 vcc, s23, v4
	s_and_saveexec_b64 s[8:9], vcc
	s_cbranch_execz .LBB0_982
	s_lshl_b32 s28, s26, 6
	s_and_b32 s28, s28, 0xffffff00
	v_and_b32_e32 v4, 0x6f, v4
	v_or_b32_e32 v4, s28, v4
	v_or_b32_e32 v5, 0x80, v4
	v_cndmask_b32_e64 v4, v4, v5, s[6:7]
	v_ashrrev_i32_e32 v5, 31, v4
	v_lshl_add_u64 v[6:7], v[4:5], 2, s[4:5]
	v_mov_b32_e32 v24, v177
	v_lshlrev_b64 v[22:23], 11, v[4:5]
	ds_read2_b32 v[6:7], v77 offset0:8 offset1:41
	ds_read2_b32 v[8:9], v77 offset0:74 offset1:107
	ds_read2_b32 v[10:11], v77 offset0:140 offset1:173
	ds_read2_b32 v[12:13], v77 offset0:206 offset1:239
	ds_read2_b32 v[14:15], v109 offset0:16 offset1:49
	ds_read2_b32 v[16:17], v109 offset0:82 offset1:115
	ds_read2_b32 v[18:19], v109 offset0:148 offset1:181
	ds_read2_b32 v[20:21], v109 offset0:214 offset1:247
	s_nop 0
	v_div_scale_f32 v25, s[28:29], v24, v24, 1.0
	v_rcp_f32_e32 v26, v25
	v_div_scale_f32 v4, vcc, 1.0, v24, 1.0
	v_fma_f32 v5, -v25, v26, 1.0
	v_fmac_f32_e32 v26, v5, v26
	v_mul_f32_e32 v5, v4, v26
	v_fma_f32 v27, -v25, v5, v4
	v_fmac_f32_e32 v5, v27, v26
	v_fma_f32 v4, -v25, v5, v4
	v_div_fmas_f32 v4, v4, v26, v5
	v_div_fixup_f32 v4, v4, v24, 1.0
	s_waitcnt lgkmcnt(7)
	v_fmaak_f32 v5, v6, v4, 0x43000000
	v_fmaak_f32 v6, v4, v7, 0x43000000
	s_waitcnt lgkmcnt(6)
	v_fmaak_f32 v7, v4, v8, 0x43000000
	v_fmaak_f32 v8, v4, v9, 0x43000000
	s_waitcnt lgkmcnt(5)
	v_fmaak_f32 v9, v4, v10, 0x43000000
	v_fmaak_f32 v10, v4, v11, 0x43000000
	s_waitcnt lgkmcnt(4)
	v_fmaak_f32 v11, v4, v12, 0x43000000
	v_fmaak_f32 v12, v4, v13, 0x43000000
	s_waitcnt lgkmcnt(3)
	v_fmaak_f32 v13, v4, v14, 0x43000000
	v_fmaak_f32 v14, v4, v15, 0x43000000
	s_waitcnt lgkmcnt(2)
	v_fmaak_f32 v15, v4, v16, 0x43000000
	v_fmaak_f32 v16, v4, v17, 0x43000000
	s_waitcnt lgkmcnt(1)
	v_fmaak_f32 v17, v4, v18, 0x43000000
	v_fmaak_f32 v18, v4, v19, 0x43000000
	v_rndne_f32_e32 v5, v5
	v_rndne_f32_e32 v9, v9
	v_rndne_f32_e32 v13, v13
	v_rndne_f32_e32 v17, v17
	s_waitcnt lgkmcnt(0)
	v_fmaak_f32 v19, v4, v20, 0x43000000
	v_rndne_f32_e32 v6, v6
	v_rndne_f32_e32 v10, v10
	v_rndne_f32_e32 v14, v14
	v_rndne_f32_e32 v18, v18
	v_cvt_pk_u8_f32 v5, v5, 0, 0
	v_cvt_pk_u8_f32 v9, v9, 0, 0
	v_cvt_pk_u8_f32 v13, v13, 0, 0
	v_cvt_pk_u8_f32 v17, v17, 0, 0
	v_fmaak_f32 v4, v4, v21, 0x43000000
	v_rndne_f32_e32 v7, v7
	v_rndne_f32_e32 v11, v11
	v_rndne_f32_e32 v15, v15
	v_rndne_f32_e32 v19, v19
	v_cvt_pk_u8_f32 v5, v6, 1, v5
	v_cvt_pk_u8_f32 v6, v10, 1, v9
	v_cvt_pk_u8_f32 v9, v14, 1, v13
	v_cvt_pk_u8_f32 v10, v18, 1, v17
	v_rndne_f32_e32 v8, v8
	v_rndne_f32_e32 v12, v12
	v_rndne_f32_e32 v16, v16
	v_rndne_f32_e32 v4, v4
	v_cvt_pk_u8_f32 v5, v7, 2, v5
	v_cvt_pk_u8_f32 v6, v11, 2, v6
	v_cvt_pk_u8_f32 v7, v15, 2, v9
	v_cvt_pk_u8_f32 v9, v19, 2, v10
	v_cvt_pk_u8_f32 v5, v8, 3, v5
	v_cvt_pk_u8_f32 v6, v12, 3, v6
	v_cvt_pk_u8_f32 v7, v16, 3, v7
	v_cvt_pk_u8_f32 v8, v4, 3, v9
	v_xor_b32_e32 v4, 0x80808080, v5
	v_xor_b32_e32 v5, 0x80808080, v6
	v_xor_b32_e32 v6, 0x80808080, v7
	v_xor_b32_e32 v7, 0x80808080, v8
	v_lshl_add_u64 v[8:9], v[2:3], 0, v[22:23]
	global_store_dwordx4 v[8:9], v[4:7], off nt
.LBB0_982:
	s_or_b64 exec, exec, s[8:9]
	s_nop 0
	v_or_b32_e32 v4, s27, v75
	v_cmp_gt_i32_e32 vcc, s23, v4
	s_and_saveexec_b64 s[8:9], vcc
	s_cbranch_execz .LBB0_984
	s_lshl_b32 s28, s26, 6
	s_and_b32 s28, s28, 0xffffff00
	v_and_b32_e32 v4, 0x77, v4
	v_or_b32_e32 v4, s28, v4
	v_or_b32_e32 v5, 0x80, v4
	v_cndmask_b32_e64 v4, v4, v5, s[6:7]
	v_ashrrev_i32_e32 v5, 31, v4
	v_lshl_add_u64 v[6:7], v[4:5], 2, s[4:5]
	v_mov_b32_e32 v24, v178
	v_lshlrev_b64 v[22:23], 11, v[4:5]
	ds_read2_b32 v[6:7], v77 offset0:16 offset1:49
	ds_read2_b32 v[8:9], v77 offset0:82 offset1:115
	ds_read2_b32 v[10:11], v77 offset0:148 offset1:181
	ds_read2_b32 v[12:13], v77 offset0:214 offset1:247
	ds_read2_b32 v[14:15], v109 offset0:24 offset1:57
	ds_read2_b32 v[16:17], v109 offset0:90 offset1:123
	ds_read2_b32 v[18:19], v109 offset0:156 offset1:189
	ds_read2_b32 v[20:21], v109 offset0:222 offset1:255
	s_nop 0
	v_div_scale_f32 v25, s[28:29], v24, v24, 1.0
	v_rcp_f32_e32 v26, v25
	v_div_scale_f32 v4, vcc, 1.0, v24, 1.0
	v_fma_f32 v5, -v25, v26, 1.0
	v_fmac_f32_e32 v26, v5, v26
	v_mul_f32_e32 v5, v4, v26
	v_fma_f32 v27, -v25, v5, v4
	v_fmac_f32_e32 v5, v27, v26
	v_fma_f32 v4, -v25, v5, v4
	v_div_fmas_f32 v4, v4, v26, v5
	v_div_fixup_f32 v4, v4, v24, 1.0
	s_waitcnt lgkmcnt(7)
	v_fmaak_f32 v5, v6, v4, 0x43000000
	v_fmaak_f32 v6, v4, v7, 0x43000000
	s_waitcnt lgkmcnt(6)
	v_fmaak_f32 v7, v4, v8, 0x43000000
	v_fmaak_f32 v8, v4, v9, 0x43000000
	s_waitcnt lgkmcnt(5)
	v_fmaak_f32 v9, v4, v10, 0x43000000
	v_fmaak_f32 v10, v4, v11, 0x43000000
	s_waitcnt lgkmcnt(4)
	v_fmaak_f32 v11, v4, v12, 0x43000000
	v_fmaak_f32 v12, v4, v13, 0x43000000
	s_waitcnt lgkmcnt(3)
	v_fmaak_f32 v13, v4, v14, 0x43000000
	v_fmaak_f32 v14, v4, v15, 0x43000000
	s_waitcnt lgkmcnt(2)
	v_fmaak_f32 v15, v4, v16, 0x43000000
	v_fmaak_f32 v16, v4, v17, 0x43000000
	s_waitcnt lgkmcnt(1)
	v_fmaak_f32 v17, v4, v18, 0x43000000
	v_fmaak_f32 v18, v4, v19, 0x43000000
	v_rndne_f32_e32 v5, v5
	v_rndne_f32_e32 v9, v9
	v_rndne_f32_e32 v13, v13
	v_rndne_f32_e32 v17, v17
	s_waitcnt lgkmcnt(0)
	v_fmaak_f32 v19, v4, v20, 0x43000000
	v_rndne_f32_e32 v6, v6
	v_rndne_f32_e32 v10, v10
	v_rndne_f32_e32 v14, v14
	v_rndne_f32_e32 v18, v18
	v_cvt_pk_u8_f32 v5, v5, 0, 0
	v_cvt_pk_u8_f32 v9, v9, 0, 0
	v_cvt_pk_u8_f32 v13, v13, 0, 0
	v_cvt_pk_u8_f32 v17, v17, 0, 0
	v_fmaak_f32 v4, v4, v21, 0x43000000
	v_rndne_f32_e32 v7, v7
	v_rndne_f32_e32 v11, v11
	v_rndne_f32_e32 v15, v15
	v_rndne_f32_e32 v19, v19
	v_cvt_pk_u8_f32 v5, v6, 1, v5
	v_cvt_pk_u8_f32 v6, v10, 1, v9
	v_cvt_pk_u8_f32 v9, v14, 1, v13
	v_cvt_pk_u8_f32 v10, v18, 1, v17
	v_rndne_f32_e32 v8, v8
	v_rndne_f32_e32 v12, v12
	v_rndne_f32_e32 v16, v16
	v_rndne_f32_e32 v4, v4
	v_cvt_pk_u8_f32 v5, v7, 2, v5
	v_cvt_pk_u8_f32 v6, v11, 2, v6
	v_cvt_pk_u8_f32 v7, v15, 2, v9
	v_cvt_pk_u8_f32 v9, v19, 2, v10
	v_cvt_pk_u8_f32 v5, v8, 3, v5
	v_cvt_pk_u8_f32 v6, v12, 3, v6
	v_cvt_pk_u8_f32 v7, v16, 3, v7
	v_cvt_pk_u8_f32 v8, v4, 3, v9
	v_xor_b32_e32 v4, 0x80808080, v5
	v_xor_b32_e32 v5, 0x80808080, v6
	v_xor_b32_e32 v6, 0x80808080, v7
	v_xor_b32_e32 v7, 0x80808080, v8
	v_lshl_add_u64 v[8:9], v[2:3], 0, v[22:23]
	global_store_dwordx4 v[8:9], v[4:7], off nt
.LBB0_984:
	s_or_b64 exec, exec, s[8:9]
	s_nop 0
	v_or_b32_e32 v4, s27, v76
	v_cmp_gt_i32_e32 vcc, s23, v4
	s_and_saveexec_b64 s[8:9], vcc
	s_cbranch_execz .LBB0_941
	s_lshl_b32 s26, s26, 6
	s_and_b32 s26, s26, 0xffffff00
	v_and_b32_e32 v4, 0x7f, v4
	v_or_b32_e32 v4, s26, v4
	v_or_b32_e32 v5, 0x80, v4
	v_cndmask_b32_e64 v4, v4, v5, s[6:7]
	v_ashrrev_i32_e32 v5, 31, v4
	v_lshl_add_u64 v[6:7], v[4:5], 2, s[4:5]
	v_mov_b32_e32 v24, v179
	v_lshlrev_b64 v[22:23], 11, v[4:5]
	ds_read2_b32 v[6:7], v77 offset0:24 offset1:57
	ds_read2_b32 v[8:9], v77 offset0:90 offset1:123
	ds_read2_b32 v[10:11], v77 offset0:156 offset1:189
	ds_read2_b32 v[12:13], v77 offset0:222 offset1:255
	ds_read2_b32 v[14:15], v109 offset0:32 offset1:65
	ds_read2_b32 v[16:17], v109 offset0:98 offset1:131
	ds_read2_b32 v[18:19], v109 offset0:164 offset1:197
	ds_read2_b32 v[20:21], v111 offset0:102 offset1:135
	v_lshl_add_u64 v[2:3], v[2:3], 0, v[22:23]
	s_nop 0
	v_div_scale_f32 v25, s[4:5], v24, v24, 1.0
	v_rcp_f32_e32 v26, v25
	v_div_scale_f32 v4, vcc, 1.0, v24, 1.0
	v_fma_f32 v5, -v25, v26, 1.0
	v_fmac_f32_e32 v26, v5, v26
	v_mul_f32_e32 v5, v4, v26
	v_fma_f32 v27, -v25, v5, v4
	v_fmac_f32_e32 v5, v27, v26
	v_fma_f32 v4, -v25, v5, v4
	v_div_fmas_f32 v4, v4, v26, v5
	v_div_fixup_f32 v4, v4, v24, 1.0
	s_waitcnt lgkmcnt(7)
	v_fmaak_f32 v5, v6, v4, 0x43000000
	v_fmaak_f32 v6, v4, v7, 0x43000000
	s_waitcnt lgkmcnt(6)
	v_fmaak_f32 v7, v4, v8, 0x43000000
	v_fmaak_f32 v8, v4, v9, 0x43000000
	s_waitcnt lgkmcnt(5)
	v_fmaak_f32 v9, v4, v10, 0x43000000
	v_fmaak_f32 v10, v4, v11, 0x43000000
	s_waitcnt lgkmcnt(4)
	v_fmaak_f32 v11, v4, v12, 0x43000000
	v_fmaak_f32 v12, v4, v13, 0x43000000
	s_waitcnt lgkmcnt(3)
	v_fmaak_f32 v13, v4, v14, 0x43000000
	v_fmaak_f32 v14, v4, v15, 0x43000000
	s_waitcnt lgkmcnt(2)
	v_fmaak_f32 v15, v4, v16, 0x43000000
	v_fmaak_f32 v16, v4, v17, 0x43000000
	s_waitcnt lgkmcnt(1)
	v_fmaak_f32 v17, v4, v18, 0x43000000
	v_fmaak_f32 v18, v4, v19, 0x43000000
	v_rndne_f32_e32 v5, v5
	v_rndne_f32_e32 v9, v9
	v_rndne_f32_e32 v13, v13
	v_rndne_f32_e32 v17, v17
	s_waitcnt lgkmcnt(0)
	v_fmaak_f32 v19, v4, v20, 0x43000000
	v_rndne_f32_e32 v6, v6
	v_rndne_f32_e32 v10, v10
	v_rndne_f32_e32 v14, v14
	v_rndne_f32_e32 v18, v18
	v_cvt_pk_u8_f32 v5, v5, 0, 0
	v_cvt_pk_u8_f32 v9, v9, 0, 0
	v_cvt_pk_u8_f32 v13, v13, 0, 0
	v_cvt_pk_u8_f32 v17, v17, 0, 0
	v_fmaak_f32 v4, v4, v21, 0x43000000
	v_rndne_f32_e32 v7, v7
	v_rndne_f32_e32 v11, v11
	v_rndne_f32_e32 v15, v15
	v_rndne_f32_e32 v19, v19
	v_cvt_pk_u8_f32 v5, v6, 1, v5
	v_cvt_pk_u8_f32 v6, v10, 1, v9
	v_cvt_pk_u8_f32 v9, v14, 1, v13
	v_cvt_pk_u8_f32 v10, v18, 1, v17
	v_rndne_f32_e32 v8, v8
	v_rndne_f32_e32 v12, v12
	v_rndne_f32_e32 v16, v16
	v_rndne_f32_e32 v4, v4
	v_cvt_pk_u8_f32 v5, v7, 2, v5
	v_cvt_pk_u8_f32 v6, v11, 2, v6
	v_cvt_pk_u8_f32 v7, v15, 2, v9
	v_cvt_pk_u8_f32 v9, v19, 2, v10
	v_cvt_pk_u8_f32 v5, v8, 3, v5
	v_cvt_pk_u8_f32 v6, v12, 3, v6
	v_cvt_pk_u8_f32 v7, v16, 3, v7
	v_cvt_pk_u8_f32 v8, v4, 3, v9
	v_xor_b32_e32 v4, 0x80808080, v5
	v_xor_b32_e32 v5, 0x80808080, v6
	v_xor_b32_e32 v6, 0x80808080, v7
	v_xor_b32_e32 v7, 0x80808080, v8
	global_store_dwordx4 v[2:3], v[4:7], off nt
	s_branch .LBB0_941

.LBB0_1288:
	s_or_b64 exec, exec, s[8:9]
	s_mul_i32 s9, s10, 0x1600000
	s_mul_hi_i32 s8, s10, 0x1600000
	s_add_u32 s29, s15, s9
	s_addc_u32 s30, s16, s8
	s_mul_i32 s8, s10, 0x2c00
	s_ashr_i32 s9, s8, 31
	s_lshl_b64 s[8:9], s[8:9], 2
	s_add_u32 s8, s17, s8
	s_addc_u32 s9, s18, s9
	v_mov_b32_e32 v181, s27
	v_lshlrev_b32_e32 v181, 6, v181
	v_and_b32_e32 v181, 0xffffff00, v181
	v_or_b32_e32 v180, s28, v73
	v_and_b32_e32 v180, 0x67, v180
	v_or_b32_e32 v180, v181, v180
	v_or_b32_e32 v182, 0x80, v180
	v_cndmask_b32_e64 v182, v180, v182, s[6:7]
	v_ashrrev_i32_e32 v183, 31, v182
	v_lshl_add_u64 v[184:185], v[182:183], 2, s[8:9]
	global_load_dword v176, v[184:185], off
	v_or_b32_e32 v180, s28, v74
	v_and_b32_e32 v180, 0x6f, v180
	v_or_b32_e32 v180, v181, v180
	v_or_b32_e32 v182, 0x80, v180
	v_cndmask_b32_e64 v182, v180, v182, s[6:7]
	v_ashrrev_i32_e32 v183, 31, v182
	v_lshl_add_u64 v[184:185], v[182:183], 2, s[8:9]
	global_load_dword v177, v[184:185], off
	v_or_b32_e32 v180, s28, v75
	v_and_b32_e32 v180, 0x77, v180
	v_or_b32_e32 v180, v181, v180
	v_or_b32_e32 v182, 0x80, v180
	v_cndmask_b32_e64 v182, v180, v182, s[6:7]
	v_ashrrev_i32_e32 v183, 31, v182
	v_lshl_add_u64 v[184:185], v[182:183], 2, s[8:9]
	global_load_dword v178, v[184:185], off
	v_or_b32_e32 v180, s28, v76
	v_and_b32_e32 v180, 0x7f, v180
	v_or_b32_e32 v180, v181, v180
	v_or_b32_e32 v182, 0x80, v180
	v_cndmask_b32_e64 v182, v180, v182, s[6:7]
	v_ashrrev_i32_e32 v183, 31, v182
	v_lshl_add_u64 v[184:185], v[182:183], 2, s[8:9]
	global_load_dword v179, v[184:185], off
	s_waitcnt vmcnt(0)
	ds_write2_b32 v78, v6, v7 offset1:1
	ds_write2_b32 v78, v8, v9 offset0:2 offset1:3
	ds_write2_b32 v79, v2, v3 offset1:1
	ds_write2_b32 v80, v4, v5 offset1:1
	ds_write2_b32 v81, v14, v15 offset1:1
	ds_write2_b32 v82, v16, v17 offset1:1
	ds_write2_b32 v83, v10, v11 offset1:1
	ds_write2_b32 v84, v12, v13 offset1:1
	ds_write2_b32 v85, v22, v23 offset1:1
	ds_write2_b32 v86, v24, v25 offset1:1
	ds_write2_b32 v87, v18, v19 offset1:1
	ds_write2_b32 v88, v20, v21 offset1:1
	ds_write2_b32 v89, v30, v31 offset1:1
	ds_write2_b32 v90, v32, v33 offset1:1
	ds_write2_b32 v91, v26, v27 offset1:1
	ds_write2_b32 v92, v28, v29 offset1:1
	ds_write2_b32 v93, v38, v39 offset1:1
	ds_write2_b32 v94, v40, v41 offset1:1
	ds_write2_b32 v95, v34, v35 offset1:1
	ds_write2_b32 v96, v36, v37 offset1:1
	ds_write2_b32 v97, v46, v47 offset1:1
	ds_write2_b32 v98, v48, v49 offset1:1
	ds_write2_b32 v99, v42, v43 offset1:1
	ds_write2_b32 v100, v44, v45 offset1:1
	ds_write2_b32 v101, v54, v55 offset1:1
	ds_write2_b32 v102, v56, v57 offset1:1
	ds_write2_b32 v103, v50, v51 offset1:1
	ds_write2_b32 v104, v52, v53 offset1:1
	ds_write2_b32 v105, v62, v63 offset1:1
	ds_write2_b32 v106, v64, v65 offset1:1
	ds_write2_b32 v107, v58, v59 offset1:1
	ds_write2_b32 v108, v60, v61 offset1:1
	s_nop 0
	s_waitcnt lgkmcnt(0)
	s_ashr_i32 s31, s11, 31
	s_add_u32 s10, s29, s11
	s_addc_u32 s11, s30, s31
	v_or_b32_e32 v4, s28, v73
	v_lshl_add_u64 v[2:3], s[10:11], 0, v[66:67]
	v_cmp_gt_i32_e32 vcc, s24, v4
	s_and_saveexec_b64 s[10:11], vcc
	s_cbranch_execz .LBB0_1290
	s_lshl_b32 s29, s27, 6
	s_and_b32 s29, s29, 0xffffff00
	v_and_b32_e32 v4, 0x67, v4
	v_or_b32_e32 v4, s29, v4
	v_or_b32_e32 v5, 0x80, v4
	v_cndmask_b32_e64 v4, v4, v5, s[6:7]
	v_ashrrev_i32_e32 v5, 31, v4
	v_lshl_add_u64 v[6:7], v[4:5], 2, s[8:9]
	v_mov_b32_e32 v24, v176
	v_lshlrev_b64 v[22:23], 11, v[4:5]
	ds_read2_b32 v[6:7], v77 offset1:33
	ds_read2_b32 v[8:9], v77 offset0:66 offset1:99
	ds_read2_b32 v[10:11], v77 offset0:132 offset1:165
	ds_read2_b32 v[12:13], v77 offset0:198 offset1:231
	ds_read2_b32 v[14:15], v109 offset0:8 offset1:41
	ds_read2_b32 v[16:17], v109 offset0:74 offset1:107
	ds_read2_b32 v[18:19], v109 offset0:140 offset1:173
	ds_read2_b32 v[20:21], v109 offset0:206 offset1:239
	s_nop 0
	v_div_scale_f32 v25, s[30:31], v24, v24, 1.0
	v_rcp_f32_e32 v26, v25
	v_div_scale_f32 v4, vcc, 1.0, v24, 1.0
	v_fma_f32 v5, -v25, v26, 1.0
	v_fmac_f32_e32 v26, v5, v26
	v_mul_f32_e32 v5, v4, v26
	v_fma_f32 v27, -v25, v5, v4
	v_fmac_f32_e32 v5, v27, v26
	v_fma_f32 v4, -v25, v5, v4
	v_div_fmas_f32 v4, v4, v26, v5
	v_div_fixup_f32 v4, v4, v24, 1.0
	s_waitcnt lgkmcnt(7)
	v_fmaak_f32 v5, v6, v4, 0x43000000
	v_fmaak_f32 v6, v4, v7, 0x43000000
	s_waitcnt lgkmcnt(6)
	v_fmaak_f32 v7, v4, v8, 0x43000000
	v_fmaak_f32 v8, v4, v9, 0x43000000
	s_waitcnt lgkmcnt(5)
	v_fmaak_f32 v9, v4, v10, 0x43000000
	v_fmaak_f32 v10, v4, v11, 0x43000000
	s_waitcnt lgkmcnt(4)
	v_fmaak_f32 v11, v4, v12, 0x43000000
	v_fmaak_f32 v12, v4, v13, 0x43000000
	s_waitcnt lgkmcnt(3)
	v_fmaak_f32 v13, v4, v14, 0x43000000
	v_fmaak_f32 v14, v4, v15, 0x43000000
	s_waitcnt lgkmcnt(2)
	v_fmaak_f32 v15, v4, v16, 0x43000000
	v_fmaak_f32 v16, v4, v17, 0x43000000
	s_waitcnt lgkmcnt(1)
	v_fmaak_f32 v17, v4, v18, 0x43000000
	v_fmaak_f32 v18, v4, v19, 0x43000000
	v_rndne_f32_e32 v5, v5
	v_rndne_f32_e32 v9, v9
	v_rndne_f32_e32 v13, v13
	v_rndne_f32_e32 v17, v17
	s_waitcnt lgkmcnt(0)
	v_fmaak_f32 v19, v4, v20, 0x43000000
	v_rndne_f32_e32 v6, v6
	v_rndne_f32_e32 v10, v10
	v_rndne_f32_e32 v14, v14
	v_rndne_f32_e32 v18, v18
	v_cvt_pk_u8_f32 v5, v5, 0, 0
	v_cvt_pk_u8_f32 v9, v9, 0, 0
	v_cvt_pk_u8_f32 v13, v13, 0, 0
	v_cvt_pk_u8_f32 v17, v17, 0, 0
	v_fmaak_f32 v4, v4, v21, 0x43000000
	v_rndne_f32_e32 v7, v7
	v_rndne_f32_e32 v11, v11
	v_rndne_f32_e32 v15, v15
	v_rndne_f32_e32 v19, v19
	v_cvt_pk_u8_f32 v5, v6, 1, v5
	v_cvt_pk_u8_f32 v6, v10, 1, v9
	v_cvt_pk_u8_f32 v9, v14, 1, v13
	v_cvt_pk_u8_f32 v10, v18, 1, v17
	v_rndne_f32_e32 v8, v8
	v_rndne_f32_e32 v12, v12
	v_rndne_f32_e32 v16, v16
	v_rndne_f32_e32 v4, v4
	v_cvt_pk_u8_f32 v5, v7, 2, v5
	v_cvt_pk_u8_f32 v6, v11, 2, v6
	v_cvt_pk_u8_f32 v7, v15, 2, v9
	v_cvt_pk_u8_f32 v9, v19, 2, v10
	v_cvt_pk_u8_f32 v5, v8, 3, v5
	v_cvt_pk_u8_f32 v6, v12, 3, v6
	v_cvt_pk_u8_f32 v7, v16, 3, v7
	v_cvt_pk_u8_f32 v8, v4, 3, v9
	v_xor_b32_e32 v4, 0x80808080, v5
	v_xor_b32_e32 v5, 0x80808080, v6
	v_xor_b32_e32 v6, 0x80808080, v7
	v_xor_b32_e32 v7, 0x80808080, v8
	v_lshl_add_u64 v[8:9], v[2:3], 0, v[22:23]
	global_store_dwordx4 v[8:9], v[4:7], off nt
.LBB0_1290:
	s_or_b64 exec, exec, s[10:11]
	s_nop 0
	v_or_b32_e32 v4, s28, v74
	v_cmp_gt_i32_e32 vcc, s24, v4
	s_and_saveexec_b64 s[10:11], vcc
	s_cbranch_execz .LBB0_1292
	s_lshl_b32 s29, s27, 6
	s_and_b32 s29, s29, 0xffffff00
	v_and_b32_e32 v4, 0x6f, v4
	v_or_b32_e32 v4, s29, v4
	v_or_b32_e32 v5, 0x80, v4
	v_cndmask_b32_e64 v4, v4, v5, s[6:7]
	v_ashrrev_i32_e32 v5, 31, v4
	v_lshl_add_u64 v[6:7], v[4:5], 2, s[8:9]
	v_mov_b32_e32 v24, v177
	v_lshlrev_b64 v[22:23], 11, v[4:5]
	ds_read2_b32 v[6:7], v77 offset0:8 offset1:41
	ds_read2_b32 v[8:9], v77 offset0:74 offset1:107
	ds_read2_b32 v[10:11], v77 offset0:140 offset1:173
	ds_read2_b32 v[12:13], v77 offset0:206 offset1:239
	ds_read2_b32 v[14:15], v109 offset0:16 offset1:49
	ds_read2_b32 v[16:17], v109 offset0:82 offset1:115
	ds_read2_b32 v[18:19], v109 offset0:148 offset1:181
	ds_read2_b32 v[20:21], v109 offset0:214 offset1:247
	s_nop 0
	v_div_scale_f32 v25, s[30:31], v24, v24, 1.0
	v_rcp_f32_e32 v26, v25
	v_div_scale_f32 v4, vcc, 1.0, v24, 1.0
	v_fma_f32 v5, -v25, v26, 1.0
	v_fmac_f32_e32 v26, v5, v26
	v_mul_f32_e32 v5, v4, v26
	v_fma_f32 v27, -v25, v5, v4
	v_fmac_f32_e32 v5, v27, v26
	v_fma_f32 v4, -v25, v5, v4
	v_div_fmas_f32 v4, v4, v26, v5
	v_div_fixup_f32 v4, v4, v24, 1.0
	s_waitcnt lgkmcnt(7)
	v_fmaak_f32 v5, v6, v4, 0x43000000
	v_fmaak_f32 v6, v4, v7, 0x43000000
	s_waitcnt lgkmcnt(6)
	v_fmaak_f32 v7, v4, v8, 0x43000000
	v_fmaak_f32 v8, v4, v9, 0x43000000
	s_waitcnt lgkmcnt(5)
	v_fmaak_f32 v9, v4, v10, 0x43000000
	v_fmaak_f32 v10, v4, v11, 0x43000000
	s_waitcnt lgkmcnt(4)
	v_fmaak_f32 v11, v4, v12, 0x43000000
	v_fmaak_f32 v12, v4, v13, 0x43000000
	s_waitcnt lgkmcnt(3)
	v_fmaak_f32 v13, v4, v14, 0x43000000
	v_fmaak_f32 v14, v4, v15, 0x43000000
	s_waitcnt lgkmcnt(2)
	v_fmaak_f32 v15, v4, v16, 0x43000000
	v_fmaak_f32 v16, v4, v17, 0x43000000
	s_waitcnt lgkmcnt(1)
	v_fmaak_f32 v17, v4, v18, 0x43000000
	v_fmaak_f32 v18, v4, v19, 0x43000000
	v_rndne_f32_e32 v5, v5
	v_rndne_f32_e32 v9, v9
	v_rndne_f32_e32 v13, v13
	v_rndne_f32_e32 v17, v17
	s_waitcnt lgkmcnt(0)
	v_fmaak_f32 v19, v4, v20, 0x43000000
	v_rndne_f32_e32 v6, v6
	v_rndne_f32_e32 v10, v10
	v_rndne_f32_e32 v14, v14
	v_rndne_f32_e32 v18, v18
	v_cvt_pk_u8_f32 v5, v5, 0, 0
	v_cvt_pk_u8_f32 v9, v9, 0, 0
	v_cvt_pk_u8_f32 v13, v13, 0, 0
	v_cvt_pk_u8_f32 v17, v17, 0, 0
	v_fmaak_f32 v4, v4, v21, 0x43000000
	v_rndne_f32_e32 v7, v7
	v_rndne_f32_e32 v11, v11
	v_rndne_f32_e32 v15, v15
	v_rndne_f32_e32 v19, v19
	v_cvt_pk_u8_f32 v5, v6, 1, v5
	v_cvt_pk_u8_f32 v6, v10, 1, v9
	v_cvt_pk_u8_f32 v9, v14, 1, v13
	v_cvt_pk_u8_f32 v10, v18, 1, v17
	v_rndne_f32_e32 v8, v8
	v_rndne_f32_e32 v12, v12
	v_rndne_f32_e32 v16, v16
	v_rndne_f32_e32 v4, v4
	v_cvt_pk_u8_f32 v5, v7, 2, v5
	v_cvt_pk_u8_f32 v6, v11, 2, v6
	v_cvt_pk_u8_f32 v7, v15, 2, v9
	v_cvt_pk_u8_f32 v9, v19, 2, v10
	v_cvt_pk_u8_f32 v5, v8, 3, v5
	v_cvt_pk_u8_f32 v6, v12, 3, v6
	v_cvt_pk_u8_f32 v7, v16, 3, v7
	v_cvt_pk_u8_f32 v8, v4, 3, v9
	v_xor_b32_e32 v4, 0x80808080, v5
	v_xor_b32_e32 v5, 0x80808080, v6
	v_xor_b32_e32 v6, 0x80808080, v7
	v_xor_b32_e32 v7, 0x80808080, v8
	v_lshl_add_u64 v[8:9], v[2:3], 0, v[22:23]
	global_store_dwordx4 v[8:9], v[4:7], off nt
.LBB0_1292:
	s_or_b64 exec, exec, s[10:11]
	s_nop 0
	v_or_b32_e32 v4, s28, v75
	v_cmp_gt_i32_e32 vcc, s24, v4
	s_and_saveexec_b64 s[10:11], vcc
	s_cbranch_execz .LBB0_1294
	s_lshl_b32 s29, s27, 6
	s_and_b32 s29, s29, 0xffffff00
	v_and_b32_e32 v4, 0x77, v4
	v_or_b32_e32 v4, s29, v4
	v_or_b32_e32 v5, 0x80, v4
	v_cndmask_b32_e64 v4, v4, v5, s[6:7]
	v_ashrrev_i32_e32 v5, 31, v4
	v_lshl_add_u64 v[6:7], v[4:5], 2, s[8:9]
	v_mov_b32_e32 v24, v178
	v_lshlrev_b64 v[22:23], 11, v[4:5]
	ds_read2_b32 v[6:7], v77 offset0:16 offset1:49
	ds_read2_b32 v[8:9], v77 offset0:82 offset1:115
	ds_read2_b32 v[10:11], v77 offset0:148 offset1:181
	ds_read2_b32 v[12:13], v77 offset0:214 offset1:247
	ds_read2_b32 v[14:15], v109 offset0:24 offset1:57
	ds_read2_b32 v[16:17], v109 offset0:90 offset1:123
	ds_read2_b32 v[18:19], v109 offset0:156 offset1:189
	ds_read2_b32 v[20:21], v109 offset0:222 offset1:255
	s_nop 0
	v_div_scale_f32 v25, s[30:31], v24, v24, 1.0
	v_rcp_f32_e32 v26, v25
	v_div_scale_f32 v4, vcc, 1.0, v24, 1.0
	v_fma_f32 v5, -v25, v26, 1.0
	v_fmac_f32_e32 v26, v5, v26
	v_mul_f32_e32 v5, v4, v26
	v_fma_f32 v27, -v25, v5, v4
	v_fmac_f32_e32 v5, v27, v26
	v_fma_f32 v4, -v25, v5, v4
	v_div_fmas_f32 v4, v4, v26, v5
	v_div_fixup_f32 v4, v4, v24, 1.0
	s_waitcnt lgkmcnt(7)
	v_fmaak_f32 v5, v6, v4, 0x43000000
	v_fmaak_f32 v6, v4, v7, 0x43000000
	s_waitcnt lgkmcnt(6)
	v_fmaak_f32 v7, v4, v8, 0x43000000
	v_fmaak_f32 v8, v4, v9, 0x43000000
	s_waitcnt lgkmcnt(5)
	v_fmaak_f32 v9, v4, v10, 0x43000000
	v_fmaak_f32 v10, v4, v11, 0x43000000
	s_waitcnt lgkmcnt(4)
	v_fmaak_f32 v11, v4, v12, 0x43000000
	v_fmaak_f32 v12, v4, v13, 0x43000000
	s_waitcnt lgkmcnt(3)
	v_fmaak_f32 v13, v4, v14, 0x43000000
	v_fmaak_f32 v14, v4, v15, 0x43000000
	s_waitcnt lgkmcnt(2)
	v_fmaak_f32 v15, v4, v16, 0x43000000
	v_fmaak_f32 v16, v4, v17, 0x43000000
	s_waitcnt lgkmcnt(1)
	v_fmaak_f32 v17, v4, v18, 0x43000000
	v_fmaak_f32 v18, v4, v19, 0x43000000
	v_rndne_f32_e32 v5, v5
	v_rndne_f32_e32 v9, v9
	v_rndne_f32_e32 v13, v13
	v_rndne_f32_e32 v17, v17
	s_waitcnt lgkmcnt(0)
	v_fmaak_f32 v19, v4, v20, 0x43000000
	v_rndne_f32_e32 v6, v6
	v_rndne_f32_e32 v10, v10
	v_rndne_f32_e32 v14, v14
	v_rndne_f32_e32 v18, v18
	v_cvt_pk_u8_f32 v5, v5, 0, 0
	v_cvt_pk_u8_f32 v9, v9, 0, 0
	v_cvt_pk_u8_f32 v13, v13, 0, 0
	v_cvt_pk_u8_f32 v17, v17, 0, 0
	v_fmaak_f32 v4, v4, v21, 0x43000000
	v_rndne_f32_e32 v7, v7
	v_rndne_f32_e32 v11, v11
	v_rndne_f32_e32 v15, v15
	v_rndne_f32_e32 v19, v19
	v_cvt_pk_u8_f32 v5, v6, 1, v5
	v_cvt_pk_u8_f32 v6, v10, 1, v9
	v_cvt_pk_u8_f32 v9, v14, 1, v13
	v_cvt_pk_u8_f32 v10, v18, 1, v17
	v_rndne_f32_e32 v8, v8
	v_rndne_f32_e32 v12, v12
	v_rndne_f32_e32 v16, v16
	v_rndne_f32_e32 v4, v4
	v_cvt_pk_u8_f32 v5, v7, 2, v5
	v_cvt_pk_u8_f32 v6, v11, 2, v6
	v_cvt_pk_u8_f32 v7, v15, 2, v9
	v_cvt_pk_u8_f32 v9, v19, 2, v10
	v_cvt_pk_u8_f32 v5, v8, 3, v5
	v_cvt_pk_u8_f32 v6, v12, 3, v6
	v_cvt_pk_u8_f32 v7, v16, 3, v7
	v_cvt_pk_u8_f32 v8, v4, 3, v9
	v_xor_b32_e32 v4, 0x80808080, v5
	v_xor_b32_e32 v5, 0x80808080, v6
	v_xor_b32_e32 v6, 0x80808080, v7
	v_xor_b32_e32 v7, 0x80808080, v8
	v_lshl_add_u64 v[8:9], v[2:3], 0, v[22:23]
	global_store_dwordx4 v[8:9], v[4:7], off nt
.LBB0_1294:
	s_or_b64 exec, exec, s[10:11]
	s_nop 0
	v_or_b32_e32 v4, s28, v76
	v_cmp_gt_i32_e32 vcc, s24, v4
	s_and_saveexec_b64 s[10:11], vcc
	s_cbranch_execz .LBB0_1251
	s_lshl_b32 s27, s27, 6
	s_and_b32 s27, s27, 0xffffff00
	v_and_b32_e32 v4, 0x7f, v4
	v_or_b32_e32 v4, s27, v4
	v_or_b32_e32 v5, 0x80, v4
	v_cndmask_b32_e64 v4, v4, v5, s[6:7]
	v_ashrrev_i32_e32 v5, 31, v4
	v_lshl_add_u64 v[6:7], v[4:5], 2, s[8:9]
	v_mov_b32_e32 v24, v179
	v_lshlrev_b64 v[22:23], 11, v[4:5]
	ds_read2_b32 v[6:7], v77 offset0:24 offset1:57
	ds_read2_b32 v[8:9], v77 offset0:90 offset1:123
	ds_read2_b32 v[10:11], v77 offset0:156 offset1:189
	ds_read2_b32 v[12:13], v77 offset0:222 offset1:255
	ds_read2_b32 v[14:15], v109 offset0:32 offset1:65
	ds_read2_b32 v[16:17], v109 offset0:98 offset1:131
	ds_read2_b32 v[18:19], v109 offset0:164 offset1:197
	ds_read2_b32 v[20:21], v111 offset0:102 offset1:135
	v_lshl_add_u64 v[2:3], v[2:3], 0, v[22:23]
	s_nop 0
	v_div_scale_f32 v25, s[6:7], v24, v24, 1.0
	v_rcp_f32_e32 v26, v25
	v_div_scale_f32 v4, vcc, 1.0, v24, 1.0
	v_fma_f32 v5, -v25, v26, 1.0
	v_fmac_f32_e32 v26, v5, v26
	v_mul_f32_e32 v5, v4, v26
	v_fma_f32 v27, -v25, v5, v4
	v_fmac_f32_e32 v5, v27, v26
	v_fma_f32 v4, -v25, v5, v4
	v_div_fmas_f32 v4, v4, v26, v5
	v_div_fixup_f32 v4, v4, v24, 1.0
	s_waitcnt lgkmcnt(7)
	v_fmaak_f32 v5, v6, v4, 0x43000000
	v_fmaak_f32 v6, v4, v7, 0x43000000
	s_waitcnt lgkmcnt(6)
	v_fmaak_f32 v7, v4, v8, 0x43000000
	v_fmaak_f32 v8, v4, v9, 0x43000000
	s_waitcnt lgkmcnt(5)
	v_fmaak_f32 v9, v4, v10, 0x43000000
	v_fmaak_f32 v10, v4, v11, 0x43000000
	s_waitcnt lgkmcnt(4)
	v_fmaak_f32 v11, v4, v12, 0x43000000
	v_fmaak_f32 v12, v4, v13, 0x43000000
	s_waitcnt lgkmcnt(3)
	v_fmaak_f32 v13, v4, v14, 0x43000000
	v_fmaak_f32 v14, v4, v15, 0x43000000
	s_waitcnt lgkmcnt(2)
	v_fmaak_f32 v15, v4, v16, 0x43000000
	v_fmaak_f32 v16, v4, v17, 0x43000000
	s_waitcnt lgkmcnt(1)
	v_fmaak_f32 v17, v4, v18, 0x43000000
	v_fmaak_f32 v18, v4, v19, 0x43000000
	v_rndne_f32_e32 v5, v5
	v_rndne_f32_e32 v9, v9
	v_rndne_f32_e32 v13, v13
	v_rndne_f32_e32 v17, v17
	s_waitcnt lgkmcnt(0)
	v_fmaak_f32 v19, v4, v20, 0x43000000
	v_rndne_f32_e32 v6, v6
	v_rndne_f32_e32 v10, v10
	v_rndne_f32_e32 v14, v14
	v_rndne_f32_e32 v18, v18
	v_cvt_pk_u8_f32 v5, v5, 0, 0
	v_cvt_pk_u8_f32 v9, v9, 0, 0
	v_cvt_pk_u8_f32 v13, v13, 0, 0
	v_cvt_pk_u8_f32 v17, v17, 0, 0
	v_fmaak_f32 v4, v4, v21, 0x43000000
	v_rndne_f32_e32 v7, v7
	v_rndne_f32_e32 v11, v11
	v_rndne_f32_e32 v15, v15
	v_rndne_f32_e32 v19, v19
	v_cvt_pk_u8_f32 v5, v6, 1, v5
	v_cvt_pk_u8_f32 v6, v10, 1, v9
	v_cvt_pk_u8_f32 v9, v14, 1, v13
	v_cvt_pk_u8_f32 v10, v18, 1, v17
	v_rndne_f32_e32 v8, v8
	v_rndne_f32_e32 v12, v12
	v_rndne_f32_e32 v16, v16
	v_rndne_f32_e32 v4, v4
	v_cvt_pk_u8_f32 v5, v7, 2, v5
	v_cvt_pk_u8_f32 v6, v11, 2, v6
	v_cvt_pk_u8_f32 v7, v15, 2, v9
	v_cvt_pk_u8_f32 v9, v19, 2, v10
	v_cvt_pk_u8_f32 v5, v8, 3, v5
	v_cvt_pk_u8_f32 v6, v12, 3, v6
	v_cvt_pk_u8_f32 v7, v16, 3, v7
	v_cvt_pk_u8_f32 v8, v4, 3, v9
	v_xor_b32_e32 v4, 0x80808080, v5
	v_xor_b32_e32 v5, 0x80808080, v6
	v_xor_b32_e32 v6, 0x80808080, v7
	v_xor_b32_e32 v7, 0x80808080, v8
	global_store_dwordx4 v[2:3], v[4:7], off nt
	s_branch .LBB0_1251

.LBB0_2083:
	s_or_b64 exec, exec, s[4:5]
	s_mul_i32 s5, s8, 0x1600000
	s_mul_hi_i32 s4, s8, 0x1600000
	s_add_u32 s28, s12, s5
	s_addc_u32 s29, s13, s4
	s_mul_i32 s4, s8, 0x2c00
	s_ashr_i32 s5, s4, 31
	s_lshl_b64 s[4:5], s[4:5], 2
	s_add_u32 s4, s14, s4
	s_addc_u32 s5, s15, s5
	v_mov_b32_e32 v181, s26
	v_lshlrev_b32_e32 v181, 6, v181
	v_and_b32_e32 v181, 0xffffff00, v181
	v_or_b32_e32 v180, s27, v73
	v_and_b32_e32 v180, 0x67, v180
	v_or_b32_e32 v180, v181, v180
	v_or_b32_e32 v182, 0x80, v180
	v_cndmask_b32_e64 v182, v180, v182, s[6:7]
	v_ashrrev_i32_e32 v183, 31, v182
	v_lshl_add_u64 v[184:185], v[182:183], 2, s[4:5]
	global_load_dword v176, v[184:185], off
	v_or_b32_e32 v180, s27, v74
	v_and_b32_e32 v180, 0x6f, v180
	v_or_b32_e32 v180, v181, v180
	v_or_b32_e32 v182, 0x80, v180
	v_cndmask_b32_e64 v182, v180, v182, s[6:7]
	v_ashrrev_i32_e32 v183, 31, v182
	v_lshl_add_u64 v[184:185], v[182:183], 2, s[4:5]
	global_load_dword v177, v[184:185], off
	v_or_b32_e32 v180, s27, v75
	v_and_b32_e32 v180, 0x77, v180
	v_or_b32_e32 v180, v181, v180
	v_or_b32_e32 v182, 0x80, v180
	v_cndmask_b32_e64 v182, v180, v182, s[6:7]
	v_ashrrev_i32_e32 v183, 31, v182
	v_lshl_add_u64 v[184:185], v[182:183], 2, s[4:5]
	global_load_dword v178, v[184:185], off
	v_or_b32_e32 v180, s27, v76
	v_and_b32_e32 v180, 0x7f, v180
	v_or_b32_e32 v180, v181, v180
	v_or_b32_e32 v182, 0x80, v180
	v_cndmask_b32_e64 v182, v180, v182, s[6:7]
	v_ashrrev_i32_e32 v183, 31, v182
	v_lshl_add_u64 v[184:185], v[182:183], 2, s[4:5]
	global_load_dword v179, v[184:185], off
	s_waitcnt vmcnt(0)
	ds_write2_b32 v78, v6, v7 offset1:1
	ds_write2_b32 v78, v8, v9 offset0:2 offset1:3
	ds_write2_b32 v79, v2, v3 offset1:1
	ds_write2_b32 v80, v4, v5 offset1:1
	ds_write2_b32 v81, v14, v15 offset1:1
	ds_write2_b32 v82, v16, v17 offset1:1
	ds_write2_b32 v83, v10, v11 offset1:1
	ds_write2_b32 v84, v12, v13 offset1:1
	ds_write2_b32 v85, v22, v23 offset1:1
	ds_write2_b32 v86, v24, v25 offset1:1
	ds_write2_b32 v87, v18, v19 offset1:1
	ds_write2_b32 v88, v20, v21 offset1:1
	ds_write2_b32 v89, v30, v31 offset1:1
	ds_write2_b32 v90, v32, v33 offset1:1
	ds_write2_b32 v91, v26, v27 offset1:1
	ds_write2_b32 v92, v28, v29 offset1:1
	ds_write2_b32 v93, v38, v39 offset1:1
	ds_write2_b32 v94, v40, v41 offset1:1
	ds_write2_b32 v95, v34, v35 offset1:1
	ds_write2_b32 v96, v36, v37 offset1:1
	ds_write2_b32 v97, v46, v47 offset1:1
	ds_write2_b32 v98, v48, v49 offset1:1
	ds_write2_b32 v99, v42, v43 offset1:1
	ds_write2_b32 v100, v44, v45 offset1:1
	ds_write2_b32 v101, v54, v55 offset1:1
	ds_write2_b32 v102, v56, v57 offset1:1
	ds_write2_b32 v103, v50, v51 offset1:1
	ds_write2_b32 v104, v52, v53 offset1:1
	ds_write2_b32 v105, v62, v63 offset1:1
	ds_write2_b32 v106, v64, v65 offset1:1
	ds_write2_b32 v107, v58, v59 offset1:1
	ds_write2_b32 v108, v60, v61 offset1:1
	s_nop 0
	s_waitcnt lgkmcnt(0)
	s_ashr_i32 s30, s9, 31
	s_add_u32 s8, s28, s9
	s_addc_u32 s9, s29, s30
	v_or_b32_e32 v4, s27, v73
	v_lshl_add_u64 v[2:3], s[8:9], 0, v[66:67]
	v_cmp_gt_i32_e32 vcc, s23, v4
	s_and_saveexec_b64 s[8:9], vcc
	s_cbranch_execz .LBB0_2085
	s_lshl_b32 s28, s26, 6
	s_and_b32 s28, s28, 0xffffff00
	v_and_b32_e32 v4, 0x67, v4
	v_or_b32_e32 v4, s28, v4
	v_or_b32_e32 v5, 0x80, v4
	v_cndmask_b32_e64 v4, v4, v5, s[6:7]
	v_ashrrev_i32_e32 v5, 31, v4
	v_lshl_add_u64 v[6:7], v[4:5], 2, s[4:5]
	v_mov_b32_e32 v24, v176
	v_lshlrev_b64 v[22:23], 11, v[4:5]
	ds_read2_b32 v[6:7], v77 offset1:33
	ds_read2_b32 v[8:9], v77 offset0:66 offset1:99
	ds_read2_b32 v[10:11], v77 offset0:132 offset1:165
	ds_read2_b32 v[12:13], v77 offset0:198 offset1:231
	ds_read2_b32 v[14:15], v109 offset0:8 offset1:41
	ds_read2_b32 v[16:17], v109 offset0:74 offset1:107
	ds_read2_b32 v[18:19], v109 offset0:140 offset1:173
	ds_read2_b32 v[20:21], v109 offset0:206 offset1:239
	s_nop 0
	v_div_scale_f32 v25, s[28:29], v24, v24, 1.0
	v_rcp_f32_e32 v26, v25
	v_div_scale_f32 v4, vcc, 1.0, v24, 1.0
	v_fma_f32 v5, -v25, v26, 1.0
	v_fmac_f32_e32 v26, v5, v26
	v_mul_f32_e32 v5, v4, v26
	v_fma_f32 v27, -v25, v5, v4
	v_fmac_f32_e32 v5, v27, v26
	v_fma_f32 v4, -v25, v5, v4
	v_div_fmas_f32 v4, v4, v26, v5
	v_div_fixup_f32 v4, v4, v24, 1.0
	s_waitcnt lgkmcnt(7)
	v_fmaak_f32 v5, v6, v4, 0x43000000
	v_fmaak_f32 v6, v4, v7, 0x43000000
	s_waitcnt lgkmcnt(6)
	v_fmaak_f32 v7, v4, v8, 0x43000000
	v_fmaak_f32 v8, v4, v9, 0x43000000
	s_waitcnt lgkmcnt(5)
	v_fmaak_f32 v9, v4, v10, 0x43000000
	v_fmaak_f32 v10, v4, v11, 0x43000000
	s_waitcnt lgkmcnt(4)
	v_fmaak_f32 v11, v4, v12, 0x43000000
	v_fmaak_f32 v12, v4, v13, 0x43000000
	s_waitcnt lgkmcnt(3)
	v_fmaak_f32 v13, v4, v14, 0x43000000
	v_fmaak_f32 v14, v4, v15, 0x43000000
	s_waitcnt lgkmcnt(2)
	v_fmaak_f32 v15, v4, v16, 0x43000000
	v_fmaak_f32 v16, v4, v17, 0x43000000
	s_waitcnt lgkmcnt(1)
	v_fmaak_f32 v17, v4, v18, 0x43000000
	v_fmaak_f32 v18, v4, v19, 0x43000000
	v_rndne_f32_e32 v5, v5
	v_rndne_f32_e32 v9, v9
	v_rndne_f32_e32 v13, v13
	v_rndne_f32_e32 v17, v17
	s_waitcnt lgkmcnt(0)
	v_fmaak_f32 v19, v4, v20, 0x43000000
	v_rndne_f32_e32 v6, v6
	v_rndne_f32_e32 v10, v10
	v_rndne_f32_e32 v14, v14
	v_rndne_f32_e32 v18, v18
	v_cvt_pk_u8_f32 v5, v5, 0, 0
	v_cvt_pk_u8_f32 v9, v9, 0, 0
	v_cvt_pk_u8_f32 v13, v13, 0, 0
	v_cvt_pk_u8_f32 v17, v17, 0, 0
	v_fmaak_f32 v4, v4, v21, 0x43000000
	v_rndne_f32_e32 v7, v7
	v_rndne_f32_e32 v11, v11
	v_rndne_f32_e32 v15, v15
	v_rndne_f32_e32 v19, v19
	v_cvt_pk_u8_f32 v5, v6, 1, v5
	v_cvt_pk_u8_f32 v6, v10, 1, v9
	v_cvt_pk_u8_f32 v9, v14, 1, v13
	v_cvt_pk_u8_f32 v10, v18, 1, v17
	v_rndne_f32_e32 v8, v8
	v_rndne_f32_e32 v12, v12
	v_rndne_f32_e32 v16, v16
	v_rndne_f32_e32 v4, v4
	v_cvt_pk_u8_f32 v5, v7, 2, v5
	v_cvt_pk_u8_f32 v6, v11, 2, v6
	v_cvt_pk_u8_f32 v7, v15, 2, v9
	v_cvt_pk_u8_f32 v9, v19, 2, v10
	v_cvt_pk_u8_f32 v5, v8, 3, v5
	v_cvt_pk_u8_f32 v6, v12, 3, v6
	v_cvt_pk_u8_f32 v7, v16, 3, v7
	v_cvt_pk_u8_f32 v8, v4, 3, v9
	v_xor_b32_e32 v4, 0x80808080, v5
	v_xor_b32_e32 v5, 0x80808080, v6
	v_xor_b32_e32 v6, 0x80808080, v7
	v_xor_b32_e32 v7, 0x80808080, v8
	v_lshl_add_u64 v[8:9], v[2:3], 0, v[22:23]
	global_store_dwordx4 v[8:9], v[4:7], off nt
